# speedup vs baseline: 1.0467x; 1.0263x over previous
.Lk1_flush:
	s_mov_b64 s[20:21], s[40:41]
	s_add_u32 s22, s20, 0x186a000
	s_addc_u32 s23, s21, 0
	s_add_u32 s24, s22, 0x186a000
	s_addc_u32 s25, s23, 0
	s_add_u32 s26, s24, 0x186a000
	s_addc_u32 s27, s25, 0
	global_store_dword v39, v56, s[20:21] sc1
	global_store_dword v39, v57, s[22:23] sc1
	global_store_dword v39, v58, s[24:25] sc1
	global_store_dword v39, v59, s[26:27] sc1
	global_store_dword v39, v60, s[20:21] offset:1024 sc1
	global_store_dword v39, v61, s[22:23] offset:1024 sc1
	global_store_dword v39, v62, s[24:25] offset:1024 sc1
	global_store_dword v39, v63, s[26:27] offset:1024 sc1
	global_store_dword v39, v64, s[20:21] offset:2048 sc1
	global_store_dword v39, v65, s[22:23] offset:2048 sc1
	global_store_dword v39, v66, s[24:25] offset:2048 sc1
	global_store_dword v39, v67, s[26:27] offset:2048 sc1
	global_store_dword v39, v68, s[20:21] offset:3072 sc1
	global_store_dword v39, v69, s[22:23] offset:3072 sc1
	global_store_dword v39, v70, s[24:25] offset:3072 sc1
	global_store_dword v39, v71, s[26:27] offset:3072 sc1
	s_add_u32 s20, s20, 0x1000
	s_addc_u32 s21, s21, 0
	s_add_u32 s22, s22, 0x1000
	s_addc_u32 s23, s23, 0
	s_add_u32 s24, s24, 0x1000
	s_addc_u32 s25, s25, 0
	s_add_u32 s26, s26, 0x1000
	s_addc_u32 s27, s27, 0
	global_store_dword v39, v72, s[20:21] sc1
	global_store_dword v39, v73, s[22:23] sc1
	global_store_dword v39, v74, s[24:25] sc1
	global_store_dword v39, v75, s[26:27] sc1
	global_store_dword v39, v76, s[20:21] offset:1024 sc1
	global_store_dword v39, v77, s[22:23] offset:1024 sc1
	global_store_dword v39, v78, s[24:25] offset:1024 sc1
	global_store_dword v39, v79, s[26:27] offset:1024 sc1
	global_store_dword v39, v80, s[20:21] offset:2048 sc1
	global_store_dword v39, v81, s[22:23] offset:2048 sc1
	global_store_dword v39, v82, s[24:25] offset:2048 sc1
	global_store_dword v39, v83, s[26:27] offset:2048 sc1
	global_store_dword v39, v84, s[20:21] offset:3072 sc1
	global_store_dword v39, v85, s[22:23] offset:3072 sc1
	global_store_dword v39, v86, s[24:25] offset:3072 sc1
	global_store_dword v39, v87, s[26:27] offset:3072 sc1
	s_add_u32 s20, s20, 0x1000
	s_addc_u32 s21, s21, 0
	s_add_u32 s22, s22, 0x1000
	s_addc_u32 s23, s23, 0
	s_add_u32 s24, s24, 0x1000
	s_addc_u32 s25, s25, 0
	s_add_u32 s26, s26, 0x1000
	s_addc_u32 s27, s27, 0
	global_store_dword v39, v88, s[20:21] sc1
	global_store_dword v39, v89, s[22:23] sc1
	global_store_dword v39, v90, s[24:25] sc1
	global_store_dword v39, v91, s[26:27] sc1
	global_store_dword v39, v92, s[20:21] offset:1024 sc1
	global_store_dword v39, v93, s[22:23] offset:1024 sc1
	global_store_dword v39, v94, s[24:25] offset:1024 sc1
	global_store_dword v39, v95, s[26:27] offset:1024 sc1
	global_store_dword v39, v96, s[20:21] offset:2048 sc1
	global_store_dword v39, v97, s[22:23] offset:2048 sc1
	global_store_dword v39, v98, s[24:25] offset:2048 sc1
	global_store_dword v39, v99, s[26:27] offset:2048 sc1
	global_store_dword v39, v100, s[20:21] offset:3072 sc1
	global_store_dword v39, v101, s[22:23] offset:3072 sc1
	global_store_dword v39, v102, s[24:25] offset:3072 sc1
	global_store_dword v39, v103, s[26:27] offset:3072 sc1
	s_add_u32 s20, s20, 0x1000
	s_addc_u32 s21, s21, 0
	s_add_u32 s22, s22, 0x1000
	s_addc_u32 s23, s23, 0
	s_add_u32 s24, s24, 0x1000
	s_addc_u32 s25, s25, 0
	s_add_u32 s26, s26, 0x1000
	s_addc_u32 s27, s27, 0
	global_store_dword v39, v104, s[20:21] sc1
	global_store_dword v39, v105, s[22:23] sc1
	global_store_dword v39, v106, s[24:25] sc1
	global_store_dword v39, v107, s[26:27] sc1
	global_store_dword v39, v108, s[20:21] offset:1024 sc1
	global_store_dword v39, v109, s[22:23] offset:1024 sc1
	global_store_dword v39, v110, s[24:25] offset:1024 sc1
	global_store_dword v39, v111, s[26:27] offset:1024 sc1
	global_store_dword v39, v112, s[20:21] offset:2048 sc1
	global_store_dword v39, v113, s[22:23] offset:2048 sc1
	global_store_dword v39, v114, s[24:25] offset:2048 sc1
	global_store_dword v39, v115, s[26:27] offset:2048 sc1
	global_store_dword v39, v116, s[20:21] offset:3072 sc1
	global_store_dword v39, v117, s[22:23] offset:3072 sc1
	global_store_dword v39, v118, s[24:25] offset:3072 sc1
	global_store_dword v39, v119, s[26:27] offset:3072 sc1
	s_add_u32 s20, s20, 0x1000
	s_addc_u32 s21, s21, 0
	s_add_u32 s22, s22, 0x1000
	s_addc_u32 s23, s23, 0
	s_add_u32 s24, s24, 0x1000
	s_addc_u32 s25, s25, 0
	s_add_u32 s26, s26, 0x1000
	s_addc_u32 s27, s27, 0
	global_store_dword v39, v120, s[20:21] sc1
	global_store_dword v39, v121, s[22:23] sc1
	global_store_dword v39, v122, s[24:25] sc1
	global_store_dword v39, v123, s[26:27] sc1
	global_store_dword v39, v124, s[20:21] offset:1024 sc1
	global_store_dword v39, v125, s[22:23] offset:1024 sc1
	global_store_dword v39, v126, s[24:25] offset:1024 sc1
	global_store_dword v39, v127, s[26:27] offset:1024 sc1
	v_mul_f32_e32 v40, 0x3c010204, v40
	v_lshlrev_b32_e32 v41, 5, v1
	s_add_u32 s15, s12, s14
	s_lshl_b32 s15, s15, 2
	s_add_u32 s8, s8, s15
	s_addc_u32 s9, s9, 0
	s_add_u32 s15, s29, 24
	v_cmp_gt_u32_e32 vcc, s15, v1
	s_and_saveexec_b64 s[38:39], vcc
	global_store_dword v41, v40, s[8:9]
	s_mov_b64 exec, s[38:39]
	s_lshl_b32 s15, s14, 12
	v_add_u32_e32 v41, s15, v34
	s_barrier
	ds_write_b128 v41, v[2:5]
	ds_write_b128 v41, v[6:9] offset:1024
	ds_write_b128 v41, v[10:13] offset:2048
	ds_write_b128 v41, v[14:17] offset:3072
	s_waitcnt lgkmcnt(0)
	s_barrier
	s_movk_i32 s15, 0x100
	v_cmp_gt_u32_e32 vcc, s15, v0
	s_and_saveexec_b64 s[38:39], vcc
	s_cbranch_execz .Lk1_end
	v_lshlrev_b32_e32 v16, 4, v0
	ds_read_b128 v[2:5], v16
	ds_read_b128 v[18:21], v16 offset:4096
	ds_read_b128 v[22:25], v16 offset:8192
	ds_read_b128 v[26:29], v16 offset:12288
	ds_read_b128 v[30:33], v16 offset:16384
	ds_read_b128 v[34:37], v16 offset:20480
	ds_read_b128 v[38:41], v16 offset:24576
	ds_read_b128 v[42:45], v16 offset:28672
	s_waitcnt lgkmcnt(6)
	v_pk_add_f32 v[2:3], v[2:3], v[18:19]
	v_pk_add_f32 v[4:5], v[4:5], v[20:21]
	s_waitcnt lgkmcnt(5)
	v_pk_add_f32 v[2:3], v[2:3], v[22:23]
	v_pk_add_f32 v[4:5], v[4:5], v[24:25]
	s_waitcnt lgkmcnt(4)
	v_pk_add_f32 v[2:3], v[2:3], v[26:27]
	v_pk_add_f32 v[4:5], v[4:5], v[28:29]
	s_waitcnt lgkmcnt(3)
	v_pk_add_f32 v[2:3], v[2:3], v[30:31]
	v_pk_add_f32 v[4:5], v[4:5], v[32:33]
	s_waitcnt lgkmcnt(2)
	v_pk_add_f32 v[2:3], v[2:3], v[34:35]
	v_pk_add_f32 v[4:5], v[4:5], v[36:37]
	s_waitcnt lgkmcnt(1)
	v_pk_add_f32 v[2:3], v[2:3], v[38:39]
	v_pk_add_f32 v[4:5], v[4:5], v[40:41]
	s_waitcnt lgkmcnt(0)
	v_pk_add_f32 v[2:3], v[2:3], v[42:43]
	v_pk_add_f32 v[4:5], v[4:5], v[44:45]
	s_lshl_b32 s15, s2, 12
	s_add_u32 s10, s10, s15
	s_addc_u32 s11, s11, 0
	global_store_dwordx4 v16, v[2:5], s[10:11]
